# v21 + nt hint on the x loads of the initial x->bf16 loop (input read once there; keeps the MALL for HB and the first layer's weights)
# baseline (speedup 1.0000x reference)
; DI unsigned pk_bf16(float lo, float hi) { const f32x2 v = {lo, hi}; return __builtin_bit_cast(unsigned, __builtin_convertvector(v, bf16x2_t)); }
; DI void phase_prologue(const Ctx& c) {
;     ...
;     for (size_t i = gt; i < (size_t)MR * 128; i += gn) {
;         const f32x4 a = *(const f32x4*)(p.x + i * 8), b = *(const f32x4*)(p.x + i * 8 + 4);
;         u32x4 w; w.x = pk_bf16(a[0], a[1]); w.y = pk_bf16(a[2], a[3]); w.z = pk_bf16(b[0], b[1]); w.w = pk_bf16(b[2], b[3]);
;         *(u32x4*)(HB + i * 8) = w;
;     }
.LBB0_54:
	global_load_dwordx4 v[10:13], v[2:3], off offset:-16 nt
	global_load_dwordx4 v[14:17], v[2:3], off nt
	v_lshl_add_u64 v[8:9], v[8:9], 0, s[4:5]
	v_cmp_lt_u64_e32 vcc, s[16:17], v[8:9]
	v_lshl_add_u64 v[2:3], v[2:3], 0, s[10:11]
	s_or_b64 s[14:15], vcc, s[14:15]
	s_waitcnt vmcnt(0)
	v_cvt_pk_bf16_f32 v10, v10, v11
	v_cvt_pk_bf16_f32 v11, v12, v13
	v_cvt_pk_bf16_f32 v12, v14, v15
	v_cvt_pk_bf16_f32 v13, v16, v17
	global_store_dwordx4 v[0:1], v[10:13], off
	v_lshl_add_u64 v[0:1], v[0:1], 0, s[8:9]
	s_andn2_b64 exec, exec, s[14:15]
	s_cbranch_execnz .LBB0_54
